# speedup vs baseline: 1.0218x; 1.0019x over previous
_Z8moe_gemmILi0EEvPKDF16_S1_PvPKyPKiPKfS1_:
	s_load_dwordx2 s[4:5], s[0:1], 0x18
	s_load_dwordx2 s[10:11], s[0:1], 0x20
	v_and_b32_e32 v1, 15, v0
	v_lshrrev_b32_e32 v2, 2, v1
	v_and_b32_e32 v3, 3, v1
	v_lshlrev_b32_e32 v2, 7, v2
	v_lshl_add_u32 v2, v3, 1, v2
	s_mov_b32 s12, 0x1c71c72
	s_waitcnt lgkmcnt(0)
	global_load_ushort v4, v2, s[4:5]
	global_load_ushort v5, v2, s[4:5] offset:512
	s_waitcnt vmcnt(0)
	s_load_dwordx4 s[4:7], s[0:1], 0x0
	v_add_u32_e32 v6, v4, v5
	v_add_u32_e32 v7, 0x8f, v6
	v_mul_hi_u32 v7, v7, s12
	v_mov_b32_e32 v8, v7
	s_nop 1
	v_add_u32_dpp v8, v8, v8 row_shr:1 row_mask:0xf bank_mask:0xf
	s_nop 1
	v_add_u32_dpp v8, v8, v8 row_shr:2 row_mask:0xf bank_mask:0xf
	s_nop 1
	v_add_u32_dpp v8, v8, v8 row_shr:4 row_mask:0xf bank_mask:0xf
	s_nop 1
	v_add_u32_dpp v8, v8, v8 row_shr:8 row_mask:0xf bank_mask:0xf
	s_nop 1
	v_readlane_b32 s15, v8, 15
	s_lshl_b32 s13, s15, 1
	s_cmp_ge_i32 s2, s13
	s_cbranch_scc1 .LBB2_132
	s_lshr_b32 s20, s15, 2
	s_and_b32 s21, s13, 6
	s_and_b32 s23, s2, 7
	s_add_i32 s24, s20, 1
	s_min_u32 s25, s23, s21
	s_mul_i32 s25, s25, s24
	s_sub_i32 s27, s23, s21
	s_max_i32 s27, s27, 0
	s_mul_i32 s27, s27, s20
	s_add_i32 s18, s25, s27
	s_ashr_i32 s28, s2, 3
	s_add_i32 s18, s18, s28
	s_ashr_i32 s22, s18, 1
	v_sub_u32_e32 v9, v8, v7
	v_cmp_le_i32_e64 s[28:29], v9, s22
	v_cmp_gt_i32_e64 s[30:31], v8, s22
	s_and_b64 s[28:29], s[28:29], s[30:31]
	s_ff1_i32_b64 s14, s[28:29]
	v_readlane_b32 s16, v4, s14
	v_readlane_b32 s17, v6, s14
	v_readlane_b32 s26, v7, s14
	v_readlane_b32 s27, v9, s14
	s_sub_i32 s2, s22, s27
